# KV up-projection GEMM epilogue: the 8 row-statistics 16-byte loads run through a 4-slot register ring (K-loop fragment registers) with counted vmcnt, instead of load-wait(0) per step
# baseline (speedup 1.0000x reference)
; __device__ __forceinline__ float dot4(f32x4 a, f32x4 b) { return (a.x * b.x + a.y * b.y) + (a.z * b.z + a.w * b.w); }
;     __device__ __forceinline__ void epi(const f32x4 (&acc)[2][2][4][2], const Unit& u, int wr, int wc, int fr, int fq) const {
;     ...
;         float sc[2][4], kr2[2][4];
; #pragma unroll
;         for (int ai = 0; ai < 2; ++ai)
; #pragma unroll
;             for (int m = 0; m < 4; ++m) { const char* q = sq + ((size_t)(ai * 128 + m * 16) * 16 + lrow * 16u) * 4;
;                 const f32x4 pk = *(const f32x4*)(q + 32); const f32x2 pr = *(const f32x2*)(q + 48);
;                 sc[ai][m] = rsqrtf(((pk.x + pk.y) + (pk.z + pk.w)) * (1.f / KVRANK) + EPS); kr2[ai][m] = pr.x + pr.y;
;                 float ss = 0.f;
; #pragma unroll
;                 for (int n = 0; n < 2; ++n) { const f32x4 y = acc[ai][0][m][n] * sc[ai][m]; ss += dot4(y, y); }
;                 ss += __shfl_xor(ss, 16); ss += __shfl_xor(ss, 32);
;                 if (fq == 0) part[(ai * 128 + m * 16 + lrow) * 4 + wc] = ss; }
.LBB0_504:
	s_lshl_b32 s46, s26, 8
	s_ashr_i32 s47, s46, 31
	s_lshl_b64 s[48:49], s[46:47], 6
	v_cmp_lt_i32_e32 vcc, v220, v215
	v_mov_b32_e32 v155, v192
	v_mov_b32_e32 v153, v190
	s_add_u32 s48, s67, s48
	v_cndmask_b32_e32 v130, v210, v220, vcc
	v_cmp_lt_i32_e32 vcc, v221, v215
	s_addc_u32 s49, s68, s49
	v_lshlrev_b32_e32 v146, 4, v153
	v_lshlrev_b32_e32 v132, 2, v130
	v_cndmask_b32_e32 v130, v210, v221, vcc
	v_lshlrev_b32_e32 v133, 2, v130
	v_lshl_add_u64 v[130:131], v[146:147], 2, s[48:49]
	global_load_dwordx2 v[184:185], v[130:131], off offset:48
	v_add_co_u32_e32 v232, vcc, 0x2000, v130
	s_nop 1
	v_addc_co_u32_e32 v233, vcc, 0, v131, vcc
	global_load_dwordx4 v[200:203], v[130:131], off offset:32
	global_load_dwordx4 v[204:207], v[130:131], off offset:1056
	global_load_dwordx4 v[216:219], v[130:131], off offset:2080
	global_load_dwordx4 v[238:241], v[130:131], off offset:3104
	s_waitcnt vmcnt(3)
	v_mov_b32_e32 v156, v201
	v_mov_b32_e32 v157, v202
	v_mov_b32_e32 v201, v203
	v_pk_add_f32 v[134:135], v[156:157], v[200:201]
	global_load_dwordx4 v[200:203], v[232:233], off offset:32
	s_nop 0
	v_add_f32_e32 v134, v134, v135
	v_fmamk_f32 v134, v134, 0x3b800000, v180
	v_cmp_gt_f32_e32 vcc, s79, v134
	v_mul_f32_e32 v135, 0x4b800000, v134
	s_nop 0
	v_cndmask_b32_e32 v134, v134, v135, vcc
	v_rsq_f32_e32 v134, v134
	s_nop 0
	v_mul_f32_e32 v135, 0x45800000, v134
	v_cndmask_b32_e32 v182, v134, v135, vcc
	v_pk_mul_f32 v[134:135], v[120:121], v[182:183] op_sel_hi:[1,0]
	v_pk_mul_f32 v[136:137], v[118:119], v[182:183] op_sel_hi:[1,0]
	v_mul_f32_e32 v135, v135, v135
	v_mul_f32_e32 v137, v137, v137
	v_fmac_f32_e32 v137, v136, v136
	v_fmac_f32_e32 v135, v134, v134
	v_add_f32_e32 v152, v137, v135
	v_pk_mul_f32 v[134:135], v[116:117], v[182:183] op_sel_hi:[1,0]
	v_pk_mul_f32 v[136:137], v[114:115], v[182:183] op_sel_hi:[1,0]
	v_mul_f32_e32 v135, v135, v135
	v_mul_f32_e32 v137, v137, v137
	v_fmac_f32_e32 v137, v136, v136
	v_fmac_f32_e32 v135, v134, v134
	v_add_f32_e32 v134, v137, v135
	v_add_f32_e32 v134, v152, v134
	ds_bpermute_b32 v135, v132, v134
	s_waitcnt lgkmcnt(0)
	v_add_f32_e32 v135, v134, v135
	ds_bpermute_b32 v136, v133, v135
	v_add_u32_e32 v134, s73, v146
	s_and_saveexec_b64 s[48:49], s[40:41]
	s_cbranch_execz .LBB0_506
	s_waitcnt lgkmcnt(0)
	v_add_f32_e32 v135, v135, v136
	ds_write_b32 v134, v135
.LBB0_506:
	s_or_b64 exec, exec, s[48:49]
	global_load_dwordx2 v[178:179], v[130:131], off offset:1072
	s_waitcnt vmcnt(4) lgkmcnt(0)
	v_mov_b32_e32 v136, v205
	v_mov_b32_e32 v137, v206
	v_mov_b32_e32 v205, v207
	v_pk_add_f32 v[136:137], v[136:137], v[204:205]
	global_load_dwordx4 v[204:207], v[232:233], off offset:1056
	s_nop 0
	v_add_f32_e32 v135, v136, v137
	v_fmamk_f32 v135, v135, 0x3b800000, v180
	v_cmp_gt_f32_e32 vcc, s79, v135
	v_mul_f32_e32 v136, 0x4b800000, v135
	s_nop 0
	v_cndmask_b32_e32 v135, v135, v136, vcc
	v_rsq_f32_e32 v135, v135
	s_nop 0
	v_mul_f32_e32 v136, 0x45800000, v135
	v_cndmask_b32_e32 v176, v135, v136, vcc
	v_pk_mul_f32 v[136:137], v[112:113], v[176:177] op_sel_hi:[1,0]
	v_pk_mul_f32 v[156:157], v[110:111], v[176:177] op_sel_hi:[1,0]
	v_mul_f32_e32 v137, v137, v137
	v_mul_f32_e32 v135, v157, v157
	v_fmac_f32_e32 v135, v156, v156
	v_fmac_f32_e32 v137, v136, v136
	v_add_f32_e32 v135, v135, v137
	v_pk_mul_f32 v[136:137], v[108:109], v[176:177] op_sel_hi:[1,0]
	v_pk_mul_f32 v[156:157], v[106:107], v[176:177] op_sel_hi:[1,0]
	v_mul_f32_e32 v137, v137, v137
	v_mul_f32_e32 v152, v157, v157
	v_fmac_f32_e32 v152, v156, v156
	v_fmac_f32_e32 v137, v136, v136
	v_add_f32_e32 v136, v152, v137
	v_add_f32_e32 v135, v135, v136
	ds_bpermute_b32 v136, v132, v135
	s_waitcnt lgkmcnt(0)
	v_add_f32_e32 v135, v135, v136
	ds_bpermute_b32 v136, v133, v135
	s_and_saveexec_b64 s[48:49], s[40:41]
	s_cbranch_execz .LBB0_508
	s_waitcnt lgkmcnt(0)
	v_add_f32_e32 v135, v135, v136
	ds_write_b32 v134, v135 offset:256
.LBB0_508:
	s_or_b64 exec, exec, s[48:49]
	global_load_dwordx2 v[174:175], v[130:131], off offset:2096
	s_waitcnt vmcnt(5) lgkmcnt(0)
	v_mov_b32_e32 v136, v217
	v_mov_b32_e32 v137, v218
	v_mov_b32_e32 v217, v219
	v_pk_add_f32 v[136:137], v[136:137], v[216:217]
	global_load_dwordx4 v[216:219], v[232:233], off offset:2080
	s_nop 0
	v_add_f32_e32 v135, v136, v137
	v_fmamk_f32 v135, v135, 0x3b800000, v180
	v_cmp_gt_f32_e32 vcc, s79, v135
	v_mul_f32_e32 v136, 0x4b800000, v135
	s_nop 0
	v_cndmask_b32_e32 v135, v135, v136, vcc
	v_rsq_f32_e32 v135, v135
	s_nop 0
	v_mul_f32_e32 v136, 0x45800000, v135
	v_cndmask_b32_e32 v172, v135, v136, vcc
	v_pk_mul_f32 v[136:137], v[96:97], v[172:173] op_sel_hi:[1,0]
	v_pk_mul_f32 v[156:157], v[94:95], v[172:173] op_sel_hi:[1,0]
	v_mul_f32_e32 v137, v137, v137
	v_mul_f32_e32 v135, v157, v157
	v_fmac_f32_e32 v135, v156, v156
	v_fmac_f32_e32 v137, v136, v136
	v_add_f32_e32 v135, v135, v137
	v_pk_mul_f32 v[136:137], v[92:93], v[172:173] op_sel_hi:[1,0]
	v_pk_mul_f32 v[156:157], v[90:91], v[172:173] op_sel_hi:[1,0]
	v_mul_f32_e32 v137, v137, v137
	v_mul_f32_e32 v152, v157, v157
	v_fmac_f32_e32 v152, v156, v156
	v_fmac_f32_e32 v137, v136, v136
	v_add_f32_e32 v136, v152, v137
	v_add_f32_e32 v135, v135, v136
	ds_bpermute_b32 v136, v132, v135
	s_waitcnt lgkmcnt(0)
	v_add_f32_e32 v135, v135, v136
	ds_bpermute_b32 v136, v133, v135
	s_and_saveexec_b64 s[48:49], s[40:41]
	s_cbranch_execz .LBB0_510
	s_waitcnt lgkmcnt(0)
	v_add_f32_e32 v135, v135, v136
	ds_write_b32 v134, v135 offset:512
; __device__ __forceinline__ float dot4(f32x4 a, f32x4 b) { return (a.x * b.x + a.y * b.y) + (a.z * b.z + a.w * b.w); }
;     __device__ __forceinline__ void epi(const f32x4 (&acc)[2][2][4][2], const Unit& u, int wr, int wc, int fr, int fq) const {
;     ...
; #pragma unroll
;         for (int ai = 0; ai < 2; ++ai)
; #pragma unroll
;             for (int m = 0; m < 4; ++m) { const char* q = sq + ((size_t)(ai * 128 + m * 16) * 16 + lrow * 16u) * 4;
;                 const f32x4 pk = *(const f32x4*)(q + 32); const f32x2 pr = *(const f32x2*)(q + 48);
;                 sc[ai][m] = rsqrtf(((pk.x + pk.y) + (pk.z + pk.w)) * (1.f / KVRANK) + EPS); kr2[ai][m] = pr.x + pr.y;
;                 float ss = 0.f;
; #pragma unroll
;                 for (int n = 0; n < 2; ++n) { const f32x4 y = acc[ai][0][m][n] * sc[ai][m]; ss += dot4(y, y); }
;                 ss += __shfl_xor(ss, 16); ss += __shfl_xor(ss, 32);
;                 if (fq == 0) part[(ai * 128 + m * 16 + lrow) * 4 + wc] = ss; }
.LBB0_510:
	s_or_b64 exec, exec, s[48:49]
	global_load_dwordx2 v[170:171], v[130:131], off offset:3120
	s_waitcnt vmcnt(6) lgkmcnt(0)
	v_mov_b32_e32 v136, v239
	v_mov_b32_e32 v137, v240
	v_mov_b32_e32 v239, v241
	v_pk_add_f32 v[136:137], v[136:137], v[238:239]
	global_load_dwordx4 v[238:241], v[232:233], off offset:3104
	s_nop 0
	v_add_f32_e32 v135, v136, v137
	v_fmamk_f32 v135, v135, 0x3b800000, v180
	v_cmp_gt_f32_e32 vcc, s79, v135
	v_mul_f32_e32 v136, 0x4b800000, v135
	s_nop 0
	v_cndmask_b32_e32 v135, v135, v136, vcc
	v_rsq_f32_e32 v135, v135
	s_nop 0
	v_mul_f32_e32 v136, 0x45800000, v135
	v_cndmask_b32_e32 v166, v135, v136, vcc
	v_pk_mul_f32 v[136:137], v[80:81], v[166:167] op_sel_hi:[1,0]
	v_pk_mul_f32 v[156:157], v[78:79], v[166:167] op_sel_hi:[1,0]
	v_mul_f32_e32 v137, v137, v137
	v_mul_f32_e32 v135, v157, v157
	v_fmac_f32_e32 v135, v156, v156
	v_fmac_f32_e32 v137, v136, v136
	v_add_f32_e32 v135, v135, v137
	v_pk_mul_f32 v[136:137], v[76:77], v[166:167] op_sel_hi:[1,0]
	v_pk_mul_f32 v[156:157], v[74:75], v[166:167] op_sel_hi:[1,0]
	v_mul_f32_e32 v137, v137, v137
	v_mul_f32_e32 v152, v157, v157
	v_fmac_f32_e32 v152, v156, v156
	v_fmac_f32_e32 v137, v136, v136
	v_add_f32_e32 v136, v152, v137
	v_add_f32_e32 v135, v135, v136
	ds_bpermute_b32 v136, v132, v135
	s_waitcnt lgkmcnt(0)
	v_add_f32_e32 v135, v135, v136
	ds_bpermute_b32 v136, v133, v135
	s_and_saveexec_b64 s[48:49], s[40:41]
	s_cbranch_execz .LBB0_512
	s_waitcnt lgkmcnt(0)
	v_add_f32_e32 v135, v135, v136
	ds_write_b32 v134, v135 offset:768
.LBB0_512:
	s_or_b64 exec, exec, s[48:49]
	v_add_co_u32_e32 v156, vcc, 0x2000, v130
	s_mov_b64 s[48:49], 0x2020
	s_nop 0
	v_addc_co_u32_e32 v157, vcc, 0, v131, vcc
	s_waitcnt lgkmcnt(0)
	v_lshl_add_u64 v[136:137], v[130:131], 0, s[48:49]
	s_nop 0
	global_load_dwordx2 v[168:169], v[136:137], off offset:16
	s_waitcnt vmcnt(7)
	v_mov_b32_e32 v136, v201
	v_mov_b32_e32 v137, v202
	v_mov_b32_e32 v201, v203
	v_pk_add_f32 v[136:137], v[136:137], v[200:201]
	s_nop 0
	v_add_f32_e32 v135, v136, v137
	v_fmamk_f32 v135, v135, 0x3b800000, v180
	v_cmp_gt_f32_e32 vcc, s79, v135
	v_mul_f32_e32 v136, 0x4b800000, v135
	s_nop 0
	v_cndmask_b32_e32 v135, v135, v136, vcc
	v_rsq_f32_e32 v135, v135
	s_nop 0
	v_mul_f32_e32 v136, 0x45800000, v135
	v_cndmask_b32_e32 v162, v135, v136, vcc
	v_pk_mul_f32 v[136:137], v[64:65], v[162:163] op_sel_hi:[1,0]
	v_pk_mul_f32 v[156:157], v[62:63], v[162:163] op_sel_hi:[1,0]
	v_mul_f32_e32 v137, v137, v137
	v_mul_f32_e32 v135, v157, v157
	v_fmac_f32_e32 v135, v156, v156
	v_fmac_f32_e32 v137, v136, v136
	v_add_f32_e32 v135, v135, v137
	v_pk_mul_f32 v[136:137], v[60:61], v[162:163] op_sel_hi:[1,0]
	v_pk_mul_f32 v[156:157], v[58:59], v[162:163] op_sel_hi:[1,0]
	v_mul_f32_e32 v137, v137, v137
	v_mul_f32_e32 v152, v157, v157
	v_fmac_f32_e32 v152, v156, v156
	v_fmac_f32_e32 v137, v136, v136
	v_add_f32_e32 v136, v152, v137
	v_add_f32_e32 v135, v135, v136
	ds_bpermute_b32 v136, v132, v135
	s_waitcnt lgkmcnt(0)
	v_add_f32_e32 v135, v135, v136
	ds_bpermute_b32 v136, v133, v135
	s_and_saveexec_b64 s[48:49], s[40:41]
	s_cbranch_execz .LBB0_514
	s_waitcnt lgkmcnt(0)
	v_add_f32_e32 v135, v135, v136
	ds_write_b32 v134, v135 offset:2048
.LBB0_514:
	s_or_b64 exec, exec, s[48:49]
	v_add_co_u32_e32 v156, vcc, 0x2000, v130
	s_mov_b64 s[48:49], 0x2420
	s_nop 0
	v_addc_co_u32_e32 v157, vcc, 0, v131, vcc
	s_waitcnt lgkmcnt(0)
	v_lshl_add_u64 v[136:137], v[130:131], 0, s[48:49]
	s_nop 0
	global_load_dwordx2 v[164:165], v[136:137], off offset:16
	s_waitcnt vmcnt(6)
	v_mov_b32_e32 v136, v205
	v_mov_b32_e32 v137, v206
	v_mov_b32_e32 v205, v207
	v_pk_add_f32 v[136:137], v[136:137], v[204:205]
	s_nop 0
	v_add_f32_e32 v135, v136, v137
	v_fmamk_f32 v135, v135, 0x3b800000, v180
	v_cmp_gt_f32_e32 vcc, s79, v135
	v_mul_f32_e32 v136, 0x4b800000, v135
	s_nop 0
	v_cndmask_b32_e32 v135, v135, v136, vcc
	v_rsq_f32_e32 v135, v135
	s_nop 0
	v_mul_f32_e32 v136, 0x45800000, v135
	v_cndmask_b32_e32 v158, v135, v136, vcc
	v_pk_mul_f32 v[136:137], v[48:49], v[158:159] op_sel_hi:[1,0]
	v_pk_mul_f32 v[156:157], v[46:47], v[158:159] op_sel_hi:[1,0]
	v_mul_f32_e32 v137, v137, v137
	v_mul_f32_e32 v135, v157, v157
	v_fmac_f32_e32 v135, v156, v156
	v_fmac_f32_e32 v137, v136, v136
	v_add_f32_e32 v135, v135, v137
	v_pk_mul_f32 v[136:137], v[44:45], v[158:159] op_sel_hi:[1,0]
	v_pk_mul_f32 v[156:157], v[42:43], v[158:159] op_sel_hi:[1,0]
	v_mul_f32_e32 v137, v137, v137
	v_mul_f32_e32 v152, v157, v157
	v_fmac_f32_e32 v152, v156, v156
	v_fmac_f32_e32 v137, v136, v136
	v_add_f32_e32 v136, v152, v137
	v_add_f32_e32 v135, v135, v136
	ds_bpermute_b32 v136, v132, v135
	s_waitcnt lgkmcnt(0)
	v_add_f32_e32 v135, v135, v136
	ds_bpermute_b32 v136, v133, v135
	s_and_saveexec_b64 s[48:49], s[40:41]
	s_cbranch_execz .LBB0_516
	s_waitcnt lgkmcnt(0)
	v_add_f32_e32 v135, v135, v136
	ds_write_b32 v134, v135 offset:2304
; __device__ __forceinline__ float dot4(f32x4 a, f32x4 b) { return (a.x * b.x + a.y * b.y) + (a.z * b.z + a.w * b.w); }
;     __device__ __forceinline__ void epi(const f32x4 (&acc)[2][2][4][2], const Unit& u, int wr, int wc, int fr, int fq) const {
;     ...
; #pragma unroll
;         for (int ai = 0; ai < 2; ++ai)
; #pragma unroll
;             for (int m = 0; m < 4; ++m) { const char* q = sq + ((size_t)(ai * 128 + m * 16) * 16 + lrow * 16u) * 4;
;                 const f32x4 pk = *(const f32x4*)(q + 32); const f32x2 pr = *(const f32x2*)(q + 48);
;                 sc[ai][m] = rsqrtf(((pk.x + pk.y) + (pk.z + pk.w)) * (1.f / KVRANK) + EPS); kr2[ai][m] = pr.x + pr.y;
;                 float ss = 0.f;
; #pragma unroll
;                 for (int n = 0; n < 2; ++n) { const f32x4 y = acc[ai][0][m][n] * sc[ai][m]; ss += dot4(y, y); }
;                 ss += __shfl_xor(ss, 16); ss += __shfl_xor(ss, 32);
;                 if (fq == 0) part[(ai * 128 + m * 16 + lrow) * 4 + wc] = ss; }
.LBB0_516:
	s_or_b64 exec, exec, s[48:49]
	v_add_co_u32_e32 v156, vcc, 0x2000, v130
	s_mov_b64 s[48:49], 0x2820
	s_nop 0
	v_addc_co_u32_e32 v157, vcc, 0, v131, vcc
	s_waitcnt lgkmcnt(0)
	v_lshl_add_u64 v[136:137], v[130:131], 0, s[48:49]
	global_load_dwordx2 v[160:161], v[136:137], off offset:16
	s_waitcnt vmcnt(5)
	v_mov_b32_e32 v136, v217
	v_mov_b32_e32 v137, v218
	v_mov_b32_e32 v217, v219
	v_pk_add_f32 v[136:137], v[136:137], v[216:217]
	s_nop 0
	v_add_f32_e32 v135, v136, v137
	v_fmamk_f32 v135, v135, 0x3b800000, v180
	v_cmp_gt_f32_e32 vcc, s79, v135
	v_mul_f32_e32 v136, 0x4b800000, v135
	s_nop 0
	v_cndmask_b32_e32 v135, v135, v136, vcc
	v_rsq_f32_e32 v135, v135
	s_nop 0
	v_mul_f32_e32 v136, 0x45800000, v135
	v_cndmask_b32_e32 v154, v135, v136, vcc
	v_pk_mul_f32 v[136:137], v[32:33], v[154:155] op_sel_hi:[1,0]
	v_pk_mul_f32 v[156:157], v[30:31], v[154:155] op_sel_hi:[1,0]
	v_mul_f32_e32 v137, v137, v137
	v_mul_f32_e32 v135, v157, v157
	v_fmac_f32_e32 v135, v156, v156
	v_fmac_f32_e32 v137, v136, v136
	v_add_f32_e32 v135, v135, v137
	v_pk_mul_f32 v[136:137], v[28:29], v[154:155] op_sel_hi:[1,0]
	v_pk_mul_f32 v[156:157], v[26:27], v[154:155] op_sel_hi:[1,0]
	v_mul_f32_e32 v137, v137, v137
	v_mul_f32_e32 v152, v157, v157
	v_fmac_f32_e32 v152, v156, v156
	v_fmac_f32_e32 v137, v136, v136
	v_add_f32_e32 v136, v152, v137
	v_add_f32_e32 v135, v135, v136
	ds_bpermute_b32 v136, v132, v135
	s_waitcnt lgkmcnt(0)
	v_add_f32_e32 v135, v135, v136
	ds_bpermute_b32 v136, v133, v135
	s_and_saveexec_b64 s[48:49], s[40:41]
	s_cbranch_execz .LBB0_518
	s_waitcnt lgkmcnt(0)
	v_add_f32_e32 v135, v135, v136
	ds_write_b32 v134, v135 offset:2560
.LBB0_518:
	s_or_b64 exec, exec, s[48:49]
	s_mov_b64 s[48:49], 0x2c20
	s_waitcnt lgkmcnt(0)
	v_lshl_add_u64 v[136:137], v[130:131], 0, s[48:49]
	v_add_co_u32_e32 v130, vcc, 0x2000, v130
	s_nop 1
	v_addc_co_u32_e32 v131, vcc, 0, v131, vcc
	global_load_dwordx2 v[156:157], v[136:137], off offset:16
	s_waitcnt vmcnt(4)
	v_mov_b32_e32 v130, v239
	v_mov_b32_e32 v131, v240
	v_mov_b32_e32 v239, v241
	v_pk_add_f32 v[130:131], v[130:131], v[238:239]
	s_nop 0
	v_add_f32_e32 v130, v130, v131
	v_fmamk_f32 v130, v130, 0x3b800000, v180
	v_cmp_gt_f32_e32 vcc, s79, v130
	v_mul_f32_e32 v131, 0x4b800000, v130
	s_nop 0
	v_cndmask_b32_e32 v130, v130, v131, vcc
	v_rsq_f32_e32 v130, v130
	s_nop 0
	v_mul_f32_e32 v131, 0x45800000, v130
	v_cndmask_b32_e32 v152, v130, v131, vcc
	v_pk_mul_f32 v[130:131], v[16:17], v[152:153] op_sel_hi:[1,0]
	v_pk_mul_f32 v[136:137], v[14:15], v[152:153] op_sel_hi:[1,0]
	v_mul_f32_e32 v131, v131, v131
	v_mul_f32_e32 v135, v137, v137
	v_fmac_f32_e32 v135, v136, v136
	v_fmac_f32_e32 v131, v130, v130
	v_add_f32_e32 v135, v135, v131
	v_pk_mul_f32 v[130:131], v[12:13], v[152:153] op_sel_hi:[1,0]
	v_pk_mul_f32 v[136:137], v[10:11], v[152:153] op_sel_hi:[1,0]
	v_mul_f32_e32 v131, v131, v131
	v_mul_f32_e32 v137, v137, v137
	v_fmac_f32_e32 v137, v136, v136
	v_fmac_f32_e32 v131, v130, v130
	v_add_f32_e32 v130, v137, v131
	v_add_f32_e32 v130, v135, v130
	ds_bpermute_b32 v131, v132, v130
	s_waitcnt lgkmcnt(0)
	v_add_f32_e32 v130, v130, v131
	ds_bpermute_b32 v131, v133, v130
	s_and_saveexec_b64 s[48:49], s[40:41]
	s_cbranch_execz .LBB0_520
	s_waitcnt lgkmcnt(0)
	v_add_f32_e32 v130, v130, v131
	ds_write_b32 v134, v130 offset:2816
